# MLA loop: wait for Q-fragment loads once before the key loop, drop the in-loop vmcnt waits that also covered the K/V prefetch
# speedup vs baseline: 1.0010x; 1.0010x over previous
; template <bool MLA>
; __device__ __forceinline__ void attn_unit(const P& p, LAS unsigned char* lds, const int b, const int h, const int qb) {
;     ...
;     bf16x8 qf[NQF];
;     { const char* qb_ = MLA ? (const char*)WSP(bf16_t, WS_QMLA) + ((size_t)(b * SEQ + qw) * 1536 + h * 192) * 2 : (const char*)WSP(bf16_t, WS_SBQ) + ((size_t)(b * SEQ + qw) * 1024 + h * 128) * 2;
;       const unsigned qo = (unsigned)((r32 * (MLA ? 1536 : 1024) + 8 * hi) * 2);
; #pragma unroll
;       for (int s = 0; s < NQF; ++s) qf[s] = *(const bf16x8*)(qb_ + qo + 32 * s); }
;     bf16x8 tri0, tri1, ones;
; #pragma unroll
;     for (int j = 0; j < 8; ++j) { const int k0_ = 8 * (j >> 2) + 4 * hi + (j & 3); tri0[j] = (k0_ > r32) ? (short)0x3F80 : (short)0; tri1[j] = (16 + k0_ > r32) ? (short)0x3F80 : (short)0; ones[j] = (short)0x3F80; }
;     u32x4 kreg[NKR], vreg[2];
;     const unsigned kofs0 = (unsigned)(((tid >> 4) * 1024 + (tid & 15) * 8) * 2), kofs1 = kofs0 + 32u * 1024u * 2u;
;     const unsigned rofs = (unsigned)(((tid >> 3) * 64 + (tid & 7) * 8) * 2);
;     const unsigned vofs0 = (unsigned)(((tid >> 3) * SEQ + (tid & 7) * 8) * 2), vofs1 = vofs0 + 64u * SEQ * 2u;
;     const unsigned kw0 = (unsigned)((tid >> 4) * KSTR + (tid & 15) * 16), kw1 = kw0 + 32u * KSTR, rw = (unsigned)((tid >> 3) * KSTR + 256 + (tid & 7) * 16);
;     const unsigned vw0 = (unsigned)(KT + (tid >> 3) * VSTR + (16 * ((tid & 7) >> 1) + 4 * (tid & 1)) * 2), vw1 = vw0 + 64u * VSTR;
;     const char* Knb = (const char*)Kn + ((size_t)b * SEQ * 1024 + h * 128) * 2; const char* Krb = (const char*)Kr + (size_t)b * SEQ * 64 * 2; const char* Vtb = (const char*)Vt;
;     ...
;     f32x16 o[4];
; #pragma unroll
;     for (int d0 = 0; d0 < 4; ++d0)
; #pragma unroll
;         for (int r = 0; r < 16; ++r) o[d0][r] = 0.f;
;     float m_run = -1e30f, l_run = 0.f, R2 = 0.f;
;     if (!MLA && tid < 8) flag[tid] = 0;
;     AT_LOAD(MLA ? 0 : nt - 1);
;     AT_WRITE(0);
;     __syncthreads();
.LBB0_705:
	v_readlane_b32 s8, v242, 40
	s_bfe_u32 s1, s2, 0x40001
	s_lshr_b32 s2, s2, 5
	v_readlane_b32 s9, v242, 41
	s_and_b64 s[8:9], s[8:9], exec
	s_cselect_b32 s1, s1, s2
	v_readfirstlane_b32 s2, v0
	s_lshl_b32 s13, s1, 8
	s_lshr_b32 s1, s2, 1
	s_and_b32 s14, s1, 0x7fffffe0
	s_sub_i32 s93, s14, s13
	s_ashr_i32 s1, s0, 31
	s_ashr_i32 s8, s0, 3
	s_and_b32 s12, s0, 7
	s_add_i32 s2, s93, 0xf00
	s_sub_i32 s9, 0x1000, s13
	s_lshl_b64 s[0:1], s[0:1], 20
	s_add_u32 s0, s88, s0
	s_addc_u32 s1, s89, s1
	s_lshl_b32 s10, s8, 12
	s_add_i32 s82, s2, s10
	s_mul_i32 s10, s82, 0x600
	s_mul_i32 s15, s12, 0xc0
	s_mul_hi_i32 s11, s82, 0x600
	s_or_b32 s10, s10, s15
	s_lshr_b32 s92, s9, 6
	s_ashr_i32 s9, s8, 31
	s_ashr_i32 s83, s82, 31
	v_lshl_add_u64 v[4:5], s[10:11], 1, v[188:189]
	s_lshl_b32 s90, s12, 7
	s_lshl_b64 s[10:11], s[8:9], 23
	s_add_u32 s10, s76, s10
	s_addc_u32 s11, s77, s11
	s_lshl_b32 s15, s14, 2
	s_add_i32 s91, s15, 0
	s_lshl_b64 s[8:9], s[8:9], 19
	s_add_i32 s91, s91, 0x16000
	s_lshl_b32 s12, s12, 8
	s_add_u32 s10, s10, s12
	s_addc_u32 s11, s11, 0
	global_load_dwordx4 v[114:117], v[4:5], off offset:32
	global_load_dwordx4 v[118:121], v[4:5], off offset:64
	global_load_dwordx4 v[122:125], v[4:5], off offset:96
	global_load_dwordx4 v[126:129], v[4:5], off offset:128
	v_lshl_add_u64 v[192:193], s[10:11], 0, v[182:183]
	s_mov_b32 s10, 0x10000
	v_add_co_u32_e32 v6, vcc, s10, v192
	v_lshl_add_u64 v[194:195], v[190:191], 0, s[8:9]
	s_nop 0
	v_addc_co_u32_e32 v7, vcc, 0, v193, vcc
	global_load_dwordx4 v[130:133], v[4:5], off offset:352
	global_load_dwordx4 v[142:145], v[6:7], off
	global_load_dwordx4 v[138:141], v[192:193], off
	global_load_dwordx4 v[170:173], v[194:195], off
	v_lshl_add_u64 v[196:197], s[0:1], 0, v[184:185]
	global_load_dwordx4 v[134:137], v[4:5], off
	global_load_dwordx4 v[174:177], v[196:197], off
	s_mov_b32 s0, 0x80000
	v_add_co_u32_e32 v6, vcc, s0, v196
	s_waitcnt vmcnt(10)
	v_mov_b32_e32 v16, v2
	v_addc_co_u32_e32 v7, vcc, 0, v197, vcc
	global_load_dwordx4 v[178:181], v[6:7], off
	global_load_dwordx4 v[146:149], v[4:5], off offset:160
	global_load_dwordx4 v[150:153], v[4:5], off offset:192
	global_load_dwordx4 v[154:157], v[4:5], off offset:224
	global_load_dwordx4 v[158:161], v[4:5], off offset:256
	global_load_dwordx4 v[162:165], v[4:5], off offset:288
	global_load_dwordx4 v[166:169], v[4:5], off offset:320
	v_mov_b32_e32 v17, v2
	v_add_u32_e32 v50, s14, v205
	v_mov_b32_e32 v3, v2
	v_mov_b32_e32 v4, v2
	v_mov_b32_e32 v5, v2
	v_mov_b32_e32 v6, v2
	v_mov_b32_e32 v7, v2
	v_mov_b32_e32 v8, v2
	v_mov_b32_e32 v9, v2
	v_mov_b32_e32 v10, v2
	v_mov_b32_e32 v11, v2
	v_mov_b32_e32 v12, v2
	v_mov_b32_e32 v13, v2
	v_mov_b32_e32 v14, v2
	v_mov_b32_e32 v15, v2
	v_mov_b64_e32 v[32:33], v[16:17]
	v_mov_b64_e32 v[48:49], v[16:17]
	v_subrev_u32_e32 v213, s13, v50
	v_mov_b64_e32 v[64:65], v[16:17]
	v_mov_b64_e32 v[80:81], v[16:17]
	s_mov_b32 s0, 0
	v_mov_b32_e32 v215, 0
	v_mov_b32_e32 v216, 0xf149f2ca
	s_mov_b32 s84, 64
	v_mov_b64_e32 v[30:31], v[14:15]
	v_mov_b64_e32 v[28:29], v[12:13]
	v_mov_b64_e32 v[26:27], v[10:11]
	v_mov_b64_e32 v[24:25], v[8:9]
	v_mov_b64_e32 v[22:23], v[6:7]
	v_mov_b64_e32 v[20:21], v[4:5]
	v_mov_b64_e32 v[18:19], v[2:3]
	v_mov_b64_e32 v[46:47], v[14:15]
	v_mov_b64_e32 v[44:45], v[12:13]
	v_mov_b64_e32 v[42:43], v[10:11]
	v_mov_b64_e32 v[40:41], v[8:9]
	v_mov_b64_e32 v[38:39], v[6:7]
	v_mov_b64_e32 v[36:37], v[4:5]
	v_mov_b64_e32 v[34:35], v[2:3]
	v_lshl_add_u32 v212, v1, 2, s91
	v_lshl_add_u32 v214, v203, 2, s91
	s_addk_i32 s93, 0xf1f
	v_mov_b64_e32 v[62:63], v[14:15]
	v_mov_b64_e32 v[60:61], v[12:13]
	v_mov_b64_e32 v[58:59], v[10:11]
	v_mov_b64_e32 v[56:57], v[8:9]
	v_mov_b64_e32 v[54:55], v[6:7]
	v_mov_b64_e32 v[52:53], v[4:5]
	v_mov_b64_e32 v[50:51], v[2:3]
	v_mov_b64_e32 v[78:79], v[14:15]
	v_mov_b64_e32 v[76:77], v[12:13]
	v_mov_b64_e32 v[74:75], v[10:11]
	v_mov_b64_e32 v[72:73], v[8:9]
	v_mov_b64_e32 v[70:71], v[6:7]
	v_mov_b64_e32 v[68:69], v[4:5]
	v_mov_b64_e32 v[66:67], v[2:3]
	s_waitcnt vmcnt(10)
	ds_write_b128 v206, v[138:141]
	ds_write_b128 v206, v[142:145] offset:12800
	s_waitcnt vmcnt(9)
	ds_write_b128 v207, v[170:173] offset:256
	s_waitcnt vmcnt(7)
	ds_write2_b64 v208, v[174:175], v[176:177] offset0:128 offset1:130
	s_waitcnt vmcnt(0)
	ds_write2_b64 v209, v[178:179], v[180:181] offset1:2
	s_waitcnt lgkmcnt(0)
	s_barrier

; #define LAS __attribute__((address_space(3)))
; #define AT_MFMA(a, b, c) __builtin_amdgcn_mfma_f32_32x32x16_bf16((a), (b), (c), 0, 0, 0)
; template <bool MLA>
; __device__ __forceinline__ void attn_unit(const P& p, LAS unsigned char* lds, const int b, const int h, const int qb) {
;     ...
;         const int tile = MLA ? it : nt - 1 - it, cb = it & 1, k0 = tile * 64;
;         const bool more = it + 1 < nt;
;         if (more) AT_LOAD(MLA ? tile + 1 : tile - 1);
;         const bool active = MLA ? (k0 <= qw + 31) : (k0 < qw + 31 && !__all(R2 < -160.f));
;         if (active) {
;             const LAS unsigned char* kb = lds + cb * BUF;
;             f32x16 p0, p1;
; #pragma unroll
;             for (int r = 0; r < 16; ++r) { p0[r] = 0.f; p1[r] = 0.f; }
; #pragma unroll
;             for (int s = 0; s < NQF; ++s) { const bf16x8 a0 = *(const LAS bf16x8*)(kb + r32 * KSTR + s * 32 + hi * 16), a1 = *(const LAS bf16x8*)(kb + (32 + r32) * KSTR + s * 32 + hi * 16);
;                 p0 = AT_MFMA(a0, qf[s], p0); p1 = AT_MFMA(a1, qf[s], p1); if ((s & 3) == 3) __builtin_amdgcn_sched_barrier(0); }
;             const int dq = qi - k0 - 4 * hi;
;             bf16x8 pf0, pf1, pf2, pf3;
;             if (MLA) {
;                 float pm = -3.0e38f;
;                 if (k0 + 63 > qw) {
; #pragma unroll
;                     for (int r = 0; r < 16; ++r) { const int c = (r & 3) + 8 * (r >> 2);
;                         if (c > dq) p0[r] = -__builtin_inff(); if (c + 32 > dq) p1[r] = -__builtin_inff(); }
.LBB0_708:
	s_and_b32 s95, s0, 1
	s_sub_i32 s0, s84, 64
	s_cmp_gt_u32 s0, s93
	s_cbranch_scc1 .LBB0_716
	s_mul_i32 s0, s95, 0xac00
	s_add_i32 s96, s0, 0
	v_add3_u32 v3, s96, v202, v198
	ds_read_b128 v[4:7], v3
	ds_read_b128 v[8:11], v3 offset:32
	s_waitcnt lgkmcnt(1)
	v_mfma_f32_32x32x16_bf16 v[82:97], v[4:7], v[134:137], 0
	ds_read_b128 v[4:7], v3 offset:12800
	ds_read_b128 v[12:15], v3 offset:12832
	s_waitcnt lgkmcnt(1)
	v_mfma_f32_32x32x16_bf16 v[98:113], v[4:7], v[134:137], 0
	v_mfma_f32_32x32x16_bf16 v[82:97], v[8:11], v[114:117], v[82:97]
	ds_read_b128 v[4:7], v3 offset:64
	ds_read_b128 v[8:11], v3 offset:96
	s_waitcnt lgkmcnt(2)
	v_mfma_f32_32x32x16_bf16 v[98:113], v[12:15], v[114:117], v[98:113]
	s_waitcnt lgkmcnt(1)
	v_mfma_f32_32x32x16_bf16 v[82:97], v[4:7], v[118:121], v[82:97]
	ds_read_b128 v[4:7], v3 offset:12864
	ds_read_b128 v[12:15], v3 offset:12896
	s_waitcnt lgkmcnt(1)
	v_mfma_f32_32x32x16_bf16 v[98:113], v[4:7], v[118:121], v[98:113]
	v_mfma_f32_32x32x16_bf16 v[82:97], v[8:11], v[122:125], v[82:97]
	s_waitcnt lgkmcnt(0)
	v_mfma_f32_32x32x16_bf16 v[98:113], v[12:15], v[122:125], v[98:113]
	ds_read_b128 v[4:7], v3 offset:128
	ds_read_b128 v[8:11], v3 offset:160
	s_waitcnt lgkmcnt(1)
	v_mfma_f32_32x32x16_bf16 v[82:97], v[4:7], v[126:129], v[82:97]
	ds_read_b128 v[4:7], v3 offset:12928
	ds_read_b128 v[12:15], v3 offset:12960
	s_waitcnt lgkmcnt(1)
	v_mfma_f32_32x32x16_bf16 v[98:113], v[4:7], v[126:129], v[98:113]
	v_mfma_f32_32x32x16_bf16 v[82:97], v[8:11], v[146:149], v[82:97]
	ds_read_b128 v[4:7], v3 offset:192
	ds_read_b128 v[8:11], v3 offset:224
	s_waitcnt lgkmcnt(2)
	v_mfma_f32_32x32x16_bf16 v[98:113], v[12:15], v[146:149], v[98:113]
	s_waitcnt lgkmcnt(1)
	v_mfma_f32_32x32x16_bf16 v[82:97], v[4:7], v[150:153], v[82:97]
	ds_read_b128 v[4:7], v3 offset:12992
	ds_read_b128 v[12:15], v3 offset:13024
	s_waitcnt lgkmcnt(1)
	v_mfma_f32_32x32x16_bf16 v[98:113], v[4:7], v[150:153], v[98:113]
	v_mfma_f32_32x32x16_bf16 v[82:97], v[8:11], v[154:157], v[82:97]
	s_waitcnt lgkmcnt(0)
	v_mfma_f32_32x32x16_bf16 v[98:113], v[12:15], v[154:157], v[98:113]
	ds_read_b128 v[4:7], v3 offset:256
	ds_read_b128 v[8:11], v3 offset:288
	s_waitcnt lgkmcnt(1)
	v_mfma_f32_32x32x16_bf16 v[82:97], v[4:7], v[158:161], v[82:97]
	ds_read_b128 v[4:7], v3 offset:13056
	ds_read_b128 v[12:15], v3 offset:13088
	s_waitcnt lgkmcnt(1)
	v_mfma_f32_32x32x16_bf16 v[98:113], v[4:7], v[158:161], v[98:113]
	v_mfma_f32_32x32x16_bf16 v[82:97], v[8:11], v[162:165], v[82:97]
	ds_read_b128 v[4:7], v3 offset:320
	ds_read_b128 v[8:11], v3 offset:352
	s_waitcnt lgkmcnt(2)
	v_mfma_f32_32x32x16_bf16 v[98:113], v[12:15], v[162:165], v[98:113]
	s_waitcnt lgkmcnt(1)
	v_mfma_f32_32x32x16_bf16 v[82:97], v[4:7], v[166:169], v[82:97]
	ds_read_b128 v[4:7], v3 offset:13120
	ds_read_b128 v[12:15], v3 offset:13152
	s_waitcnt lgkmcnt(1)
	v_mfma_f32_32x32x16_bf16 v[98:113], v[4:7], v[166:169], v[98:113]
	v_mfma_f32_32x32x16_bf16 v[82:97], v[8:11], v[130:133], v[82:97]
	s_waitcnt lgkmcnt(0)
	v_mfma_f32_32x32x16_bf16 v[98:113], v[12:15], v[130:133], v[98:113]
	s_add_i32 s0, s84, -1
	s_cmp_le_u32 s0, s2
	s_cbranch_scc1 .LBB0_711
	v_cmp_gt_i32_e64 s[66:67], 26, v213
	v_cmp_gt_i32_e64 s[68:69], 27, v213
	v_cmp_gt_i32_e64 s[64:65], 25, v213
	s_and_b64 s[66:67], s[68:69], s[66:67]
	v_cmp_gt_i32_e64 s[62:63], 24, v213
	s_and_b64 s[64:65], s[66:67], s[64:65]
	v_cmp_gt_i32_e64 s[60:61], 19, v213
	s_and_b64 s[62:63], s[64:65], s[62:63]
	v_cmp_gt_i32_e64 s[58:59], 18, v213
	s_and_b64 s[60:61], s[62:63], s[60:61]
	v_cmp_gt_i32_e64 s[56:57], 17, v213
	s_and_b64 s[58:59], s[60:61], s[58:59]
	v_cmp_gt_i32_e64 s[54:55], 16, v213
	s_and_b64 s[56:57], s[58:59], s[56:57]
	v_cmp_gt_i32_e64 s[52:53], 11, v213
	s_and_b64 s[54:55], s[56:57], s[54:55]
	v_cmp_gt_i32_e64 s[50:51], 10, v213
	s_and_b64 s[52:53], s[54:55], s[52:53]
	v_cmp_gt_i32_e64 s[48:49], 9, v213
	s_and_b64 s[50:51], s[52:53], s[50:51]
	v_cmp_gt_i32_e64 s[46:47], 8, v213
	s_and_b64 s[48:49], s[50:51], s[48:49]
	v_cmp_gt_i32_e64 s[44:45], 3, v213
	s_and_b64 s[46:47], s[48:49], s[46:47]
	v_cmp_gt_i32_e64 s[42:43], 2, v213
	s_and_b64 s[44:45], s[46:47], s[44:45]
	v_cmp_gt_i32_e64 s[38:39], 1, v213
	s_and_b64 s[42:43], s[44:45], s[42:43]
	v_cmp_gt_i32_e64 s[0:1], 0, v213
	s_and_b64 s[38:39], s[42:43], s[38:39]
	s_and_b64 s[0:1], s[38:39], s[0:1]
	v_cmp_gt_i32_e64 s[36:37], 58, v213
	v_cndmask_b32_e64 v82, v82, v210, s[0:1]
	v_cmp_gt_i32_e64 s[0:1], 59, v213
	v_cmp_gt_i32_e64 s[34:35], 57, v213
	v_cmp_gt_i32_e64 s[30:31], 56, v213
	v_cndmask_b32_e64 v113, v113, v210, s[0:1]
	s_and_b64 s[0:1], s[0:1], s[36:37]
	v_cndmask_b32_e64 v112, v112, v210, s[0:1]
	s_and_b64 s[0:1], s[0:1], s[34:35]
	v_cmp_gt_i32_e64 s[28:29], 51, v213
	v_cndmask_b32_e64 v111, v111, v210, s[0:1]
	s_and_b64 s[0:1], s[0:1], s[30:31]
	v_cmp_gt_i32_e64 s[26:27], 50, v213
	v_cndmask_b32_e64 v110, v110, v210, s[0:1]
	s_and_b64 s[0:1], s[0:1], s[28:29]
	v_cmp_gt_i32_e64 s[24:25], 49, v213
	v_cndmask_b32_e64 v109, v109, v210, s[0:1]
	s_and_b64 s[0:1], s[0:1], s[26:27]
	v_cmp_gt_i32_e64 s[22:23], 48, v213
	v_cndmask_b32_e64 v108, v108, v210, s[0:1]
	s_and_b64 s[0:1], s[0:1], s[24:25]
	v_cmp_gt_i32_e64 s[20:21], 43, v213
	v_cndmask_b32_e64 v107, v107, v210, s[0:1]
	s_and_b64 s[0:1], s[0:1], s[22:23]
	v_cmp_gt_i32_e64 s[18:19], 42, v213
	v_cndmask_b32_e64 v106, v106, v210, s[0:1]
	s_and_b64 s[0:1], s[0:1], s[20:21]
	v_cmp_gt_i32_e64 s[16:17], 41, v213
	v_cndmask_b32_e64 v105, v105, v210, s[0:1]
	s_and_b64 s[0:1], s[0:1], s[18:19]
	v_cmp_gt_i32_e64 s[14:15], 40, v213
	v_cndmask_b32_e64 v104, v104, v210, s[0:1]
	s_and_b64 s[0:1], s[0:1], s[16:17]
	v_cmp_gt_i32_e64 s[12:13], 35, v213
	v_cndmask_b32_e64 v103, v103, v210, s[0:1]
	s_and_b64 s[0:1], s[0:1], s[14:15]
	v_cmp_gt_i32_e64 s[10:11], 34, v213
	v_cndmask_b32_e64 v102, v102, v210, s[0:1]
	s_and_b64 s[0:1], s[0:1], s[12:13]
	v_cmp_gt_i32_e64 s[8:9], 33, v213
	v_cndmask_b32_e64 v101, v101, v210, s[0:1]
	s_and_b64 s[0:1], s[0:1], s[10:11]
	v_cmp_gt_i32_e32 vcc, 32, v213
	v_cndmask_b32_e64 v100, v100, v210, s[0:1]
	s_and_b64 s[0:1], s[0:1], s[8:9]
	s_and_b64 vcc, s[0:1], vcc
	v_cndmask_b32_e64 v97, v97, v210, s[68:69]
	v_cndmask_b32_e64 v96, v96, v210, s[66:67]
	v_cndmask_b32_e64 v95, v95, v210, s[64:65]
	v_cndmask_b32_e64 v94, v94, v210, s[62:63]
	v_cndmask_b32_e64 v93, v93, v210, s[60:61]
	v_cndmask_b32_e64 v92, v92, v210, s[58:59]
	v_cndmask_b32_e64 v91, v91, v210, s[56:57]
	v_cndmask_b32_e64 v90, v90, v210, s[54:55]
	v_cndmask_b32_e64 v89, v89, v210, s[52:53]
	v_cndmask_b32_e64 v88, v88, v210, s[50:51]
	v_cndmask_b32_e64 v87, v87, v210, s[48:49]
	v_cndmask_b32_e64 v86, v86, v210, s[46:47]
	v_cndmask_b32_e64 v85, v85, v210, s[44:45]
	v_cndmask_b32_e64 v84, v84, v210, s[42:43]
	v_cndmask_b32_e64 v83, v83, v210, s[38:39]
	v_cndmask_b32_e64 v99, v99, v210, s[0:1]
	v_cndmask_b32_e32 v98, v98, v210, vcc

; template <bool MLA>
; __device__ __forceinline__ void attn_unit(const P& p, LAS unsigned char* lds, const int b, const int h, const int qb) {
;     ...
;     bf16x8 qf[NQF];
;     { const char* qb_ = MLA ? (const char*)WSP(bf16_t, WS_QMLA) + ((size_t)(b * SEQ + qw) * 1536 + h * 192) * 2 : (const char*)WSP(bf16_t, WS_SBQ) + ((size_t)(b * SEQ + qw) * 1024 + h * 128) * 2;
;       const unsigned qo = (unsigned)((r32 * (MLA ? 1536 : 1024) + 8 * hi) * 2);
; #pragma unroll
;       for (int s = 0; s < NQF; ++s) qf[s] = *(const bf16x8*)(qb_ + qo + 32 * s); }
;     bf16x8 tri0, tri1, ones;
; #pragma unroll
;     for (int j = 0; j < 8; ++j) { const int k0_ = 8 * (j >> 2) + 4 * hi + (j & 3); tri0[j] = (k0_ > r32) ? (short)0x3F80 : (short)0; tri1[j] = (16 + k0_ > r32) ? (short)0x3F80 : (short)0; ones[j] = (short)0x3F80; }
;     u32x4 kreg[NKR], vreg[2];
;     const unsigned kofs0 = (unsigned)(((tid >> 4) * 1024 + (tid & 15) * 8) * 2), kofs1 = kofs0 + 32u * 1024u * 2u;
;     const unsigned rofs = (unsigned)(((tid >> 3) * 64 + (tid & 7) * 8) * 2);
;     const unsigned vofs0 = (unsigned)(((tid >> 3) * SEQ + (tid & 7) * 8) * 2), vofs1 = vofs0 + 64u * SEQ * 2u;
;     const unsigned kw0 = (unsigned)((tid >> 4) * KSTR + (tid & 15) * 16), kw1 = kw0 + 32u * KSTR, rw = (unsigned)((tid >> 3) * KSTR + 256 + (tid & 7) * 16);
;     const unsigned vw0 = (unsigned)(KT + (tid >> 3) * VSTR + (16 * ((tid & 7) >> 1) + 4 * (tid & 1)) * 2), vw1 = vw0 + 64u * VSTR;
;     const char* Knb = (const char*)Kn + ((size_t)b * SEQ * 1024 + h * 128) * 2; const char* Krb = (const char*)Kr + (size_t)b * SEQ * 64 * 2; const char* Vtb = (const char*)Vt;
;     ...
;     f32x16 o[4];
; #pragma unroll
;     for (int d0 = 0; d0 < 4; ++d0)
; #pragma unroll
;         for (int r = 0; r < 16; ++r) o[d0][r] = 0.f;
;     float m_run = -1e30f, l_run = 0.f, R2 = 0.f;
;     if (!MLA && tid < 8) flag[tid] = 0;
;     AT_LOAD(MLA ? 0 : nt - 1);
;     AT_WRITE(0);
;     __syncthreads();
.LBB0_871:
	v_readlane_b32 s8, v242, 40
	s_bfe_u32 s1, s2, 0x40001
	s_lshr_b32 s2, s2, 5
	v_readlane_b32 s9, v242, 41
	s_and_b64 s[8:9], s[8:9], exec
	s_cselect_b32 s1, s1, s2
	v_readfirstlane_b32 s2, v0
	s_lshl_b32 s13, s1, 8
	s_lshr_b32 s1, s2, 1
	s_and_b32 s14, s1, 0x7fffffe0
	s_sub_i32 s93, s14, s13
	s_ashr_i32 s1, s0, 31
	s_ashr_i32 s8, s0, 3
	s_and_b32 s12, s0, 7
	s_add_i32 s2, s93, 0xf00
	s_sub_i32 s9, 0x1000, s13
	s_lshl_b64 s[0:1], s[0:1], 20
	s_add_u32 s0, s88, s0
	s_addc_u32 s1, s89, s1
	s_lshl_b32 s10, s8, 12
	s_add_i32 s82, s2, s10
	s_mul_i32 s10, s82, 0x600
	s_mul_i32 s15, s12, 0xc0
	s_mul_hi_i32 s11, s82, 0x600
	s_or_b32 s10, s10, s15
	s_lshr_b32 s92, s9, 6
	s_ashr_i32 s9, s8, 31
	s_ashr_i32 s83, s82, 31
	v_lshl_add_u64 v[4:5], s[10:11], 1, v[188:189]
	s_lshl_b32 s90, s12, 7
	s_lshl_b64 s[10:11], s[8:9], 23
	s_add_u32 s10, s76, s10
	s_addc_u32 s11, s77, s11
	s_lshl_b32 s15, s14, 2
	s_add_i32 s91, s15, 0
	s_lshl_b64 s[8:9], s[8:9], 19
	s_add_i32 s91, s91, 0x16000
	s_lshl_b32 s12, s12, 8
	s_add_u32 s10, s10, s12
	s_addc_u32 s11, s11, 0
	global_load_dwordx4 v[114:117], v[4:5], off offset:32
	global_load_dwordx4 v[118:121], v[4:5], off offset:64
	global_load_dwordx4 v[122:125], v[4:5], off offset:96
	global_load_dwordx4 v[126:129], v[4:5], off offset:128
	v_lshl_add_u64 v[192:193], s[10:11], 0, v[182:183]
	s_mov_b32 s10, 0x10000
	v_add_co_u32_e32 v6, vcc, s10, v192
	v_lshl_add_u64 v[194:195], v[190:191], 0, s[8:9]
	s_nop 0
	v_addc_co_u32_e32 v7, vcc, 0, v193, vcc
	global_load_dwordx4 v[130:133], v[4:5], off offset:352
	global_load_dwordx4 v[142:145], v[6:7], off
	global_load_dwordx4 v[138:141], v[192:193], off
	global_load_dwordx4 v[170:173], v[194:195], off
	v_lshl_add_u64 v[196:197], s[0:1], 0, v[184:185]
	global_load_dwordx4 v[134:137], v[4:5], off
	global_load_dwordx4 v[174:177], v[196:197], off
	s_mov_b32 s0, 0x80000
	v_add_co_u32_e32 v6, vcc, s0, v196
	s_waitcnt vmcnt(10)
	v_mov_b32_e32 v16, v2
	v_addc_co_u32_e32 v7, vcc, 0, v197, vcc
	global_load_dwordx4 v[178:181], v[6:7], off
	global_load_dwordx4 v[146:149], v[4:5], off offset:160
	global_load_dwordx4 v[150:153], v[4:5], off offset:192
	global_load_dwordx4 v[154:157], v[4:5], off offset:224
	global_load_dwordx4 v[158:161], v[4:5], off offset:256
	global_load_dwordx4 v[162:165], v[4:5], off offset:288
	global_load_dwordx4 v[166:169], v[4:5], off offset:320
	v_mov_b32_e32 v17, v2
	v_add_u32_e32 v50, s14, v208
	v_mov_b32_e32 v3, v2
	v_mov_b32_e32 v4, v2
	v_mov_b32_e32 v5, v2
	v_mov_b32_e32 v6, v2
	v_mov_b32_e32 v7, v2
	v_mov_b32_e32 v8, v2
	v_mov_b32_e32 v9, v2
	v_mov_b32_e32 v10, v2
	v_mov_b32_e32 v11, v2
	v_mov_b32_e32 v12, v2
	v_mov_b32_e32 v13, v2
	v_mov_b32_e32 v14, v2
	v_mov_b32_e32 v15, v2
	v_mov_b64_e32 v[32:33], v[16:17]
	v_mov_b64_e32 v[48:49], v[16:17]
	v_subrev_u32_e32 v216, s13, v50
	v_mov_b64_e32 v[64:65], v[16:17]
	v_mov_b64_e32 v[80:81], v[16:17]
	s_mov_b32 s0, 0
	v_mov_b32_e32 v218, 0
	v_mov_b32_e32 v219, 0xf149f2ca
	s_mov_b32 s84, 64
	v_mov_b64_e32 v[30:31], v[14:15]
	v_mov_b64_e32 v[28:29], v[12:13]
	v_mov_b64_e32 v[26:27], v[10:11]
	v_mov_b64_e32 v[24:25], v[8:9]
	v_mov_b64_e32 v[22:23], v[6:7]
	v_mov_b64_e32 v[20:21], v[4:5]
	v_mov_b64_e32 v[18:19], v[2:3]
	v_mov_b64_e32 v[46:47], v[14:15]
	v_mov_b64_e32 v[44:45], v[12:13]
	v_mov_b64_e32 v[42:43], v[10:11]
	v_mov_b64_e32 v[40:41], v[8:9]
	v_mov_b64_e32 v[38:39], v[6:7]
	v_mov_b64_e32 v[36:37], v[4:5]
	v_mov_b64_e32 v[34:35], v[2:3]
	v_lshl_add_u32 v215, v1, 2, s91
	v_lshl_add_u32 v217, v206, 2, s91
	s_addk_i32 s93, 0xf1f
	v_mov_b64_e32 v[62:63], v[14:15]
	v_mov_b64_e32 v[60:61], v[12:13]
	v_mov_b64_e32 v[58:59], v[10:11]
	v_mov_b64_e32 v[56:57], v[8:9]
	v_mov_b64_e32 v[54:55], v[6:7]
	v_mov_b64_e32 v[52:53], v[4:5]
	v_mov_b64_e32 v[50:51], v[2:3]
	v_mov_b64_e32 v[78:79], v[14:15]
	v_mov_b64_e32 v[76:77], v[12:13]
	v_mov_b64_e32 v[74:75], v[10:11]
	v_mov_b64_e32 v[72:73], v[8:9]
	v_mov_b64_e32 v[70:71], v[6:7]
	v_mov_b64_e32 v[68:69], v[4:5]
	v_mov_b64_e32 v[66:67], v[2:3]
	s_waitcnt vmcnt(10)
	ds_write_b128 v209, v[138:141]
	ds_write_b128 v209, v[142:145] offset:12800
	s_waitcnt vmcnt(9)
	ds_write_b128 v210, v[170:173] offset:256
	s_waitcnt vmcnt(7)
	ds_write2_b64 v211, v[174:175], v[176:177] offset0:128 offset1:130
	s_waitcnt vmcnt(0)
	ds_write2_b64 v212, v[178:179], v[180:181] offset1:2
	s_waitcnt lgkmcnt(0)
	s_barrier

; #define LAS __attribute__((address_space(3)))
; #define AT_MFMA(a, b, c) __builtin_amdgcn_mfma_f32_32x32x16_bf16((a), (b), (c), 0, 0, 0)
; template <bool MLA>
; __device__ __forceinline__ void attn_unit(const P& p, LAS unsigned char* lds, const int b, const int h, const int qb) {
;     ...
;         const int tile = MLA ? it : nt - 1 - it, cb = it & 1, k0 = tile * 64;
;         const bool more = it + 1 < nt;
;         if (more) AT_LOAD(MLA ? tile + 1 : tile - 1);
;         const bool active = MLA ? (k0 <= qw + 31) : (k0 < qw + 31 && !__all(R2 < -160.f));
;         if (active) {
;             const LAS unsigned char* kb = lds + cb * BUF;
;             f32x16 p0, p1;
; #pragma unroll
;             for (int r = 0; r < 16; ++r) { p0[r] = 0.f; p1[r] = 0.f; }
; #pragma unroll
;             for (int s = 0; s < NQF; ++s) { const bf16x8 a0 = *(const LAS bf16x8*)(kb + r32 * KSTR + s * 32 + hi * 16), a1 = *(const LAS bf16x8*)(kb + (32 + r32) * KSTR + s * 32 + hi * 16);
;                 p0 = AT_MFMA(a0, qf[s], p0); p1 = AT_MFMA(a1, qf[s], p1); if ((s & 3) == 3) __builtin_amdgcn_sched_barrier(0); }
;             const int dq = qi - k0 - 4 * hi;
;             bf16x8 pf0, pf1, pf2, pf3;
;             if (MLA) {
;                 float pm = -3.0e38f;
;                 if (k0 + 63 > qw) {
; #pragma unroll
;                     for (int r = 0; r < 16; ++r) { const int c = (r & 3) + 8 * (r >> 2);
;                         if (c > dq) p0[r] = -__builtin_inff(); if (c + 32 > dq) p1[r] = -__builtin_inff(); }
.LBB0_874:
	s_and_b32 s95, s0, 1
	s_sub_i32 s0, s84, 64
	s_cmp_gt_u32 s0, s93
	s_cbranch_scc1 .LBB0_882
	s_mul_i32 s0, s95, 0xac00
	s_add_i32 s96, s0, 0
	v_add3_u32 v3, s96, v205, v201
	ds_read_b128 v[4:7], v3
	ds_read_b128 v[8:11], v3 offset:32
	s_waitcnt lgkmcnt(1)
	v_mfma_f32_32x32x16_bf16 v[82:97], v[4:7], v[134:137], 0
	ds_read_b128 v[4:7], v3 offset:12800
	ds_read_b128 v[12:15], v3 offset:12832
	s_waitcnt lgkmcnt(1)
	v_mfma_f32_32x32x16_bf16 v[98:113], v[4:7], v[134:137], 0
	v_mfma_f32_32x32x16_bf16 v[82:97], v[8:11], v[114:117], v[82:97]
	ds_read_b128 v[4:7], v3 offset:64
	ds_read_b128 v[8:11], v3 offset:96
	s_waitcnt lgkmcnt(2)
	v_mfma_f32_32x32x16_bf16 v[98:113], v[12:15], v[114:117], v[98:113]
	s_waitcnt lgkmcnt(1)
	v_mfma_f32_32x32x16_bf16 v[82:97], v[4:7], v[118:121], v[82:97]
	ds_read_b128 v[4:7], v3 offset:12864
	ds_read_b128 v[12:15], v3 offset:12896
	s_waitcnt lgkmcnt(1)
	v_mfma_f32_32x32x16_bf16 v[98:113], v[4:7], v[118:121], v[98:113]
	v_mfma_f32_32x32x16_bf16 v[82:97], v[8:11], v[122:125], v[82:97]
	s_waitcnt lgkmcnt(0)
	v_mfma_f32_32x32x16_bf16 v[98:113], v[12:15], v[122:125], v[98:113]
	ds_read_b128 v[4:7], v3 offset:128
	ds_read_b128 v[8:11], v3 offset:160
	s_waitcnt lgkmcnt(1)
	v_mfma_f32_32x32x16_bf16 v[82:97], v[4:7], v[126:129], v[82:97]
	ds_read_b128 v[4:7], v3 offset:12928
	ds_read_b128 v[12:15], v3 offset:12960
	s_waitcnt lgkmcnt(1)
	v_mfma_f32_32x32x16_bf16 v[98:113], v[4:7], v[126:129], v[98:113]
	v_mfma_f32_32x32x16_bf16 v[82:97], v[8:11], v[146:149], v[82:97]
	ds_read_b128 v[4:7], v3 offset:192
	ds_read_b128 v[8:11], v3 offset:224
	s_waitcnt lgkmcnt(2)
	v_mfma_f32_32x32x16_bf16 v[98:113], v[12:15], v[146:149], v[98:113]
	s_waitcnt lgkmcnt(1)
	v_mfma_f32_32x32x16_bf16 v[82:97], v[4:7], v[150:153], v[82:97]
	ds_read_b128 v[4:7], v3 offset:12992
	ds_read_b128 v[12:15], v3 offset:13024
	s_waitcnt lgkmcnt(1)
	v_mfma_f32_32x32x16_bf16 v[98:113], v[4:7], v[150:153], v[98:113]
	v_mfma_f32_32x32x16_bf16 v[82:97], v[8:11], v[154:157], v[82:97]
	s_waitcnt lgkmcnt(0)
	v_mfma_f32_32x32x16_bf16 v[98:113], v[12:15], v[154:157], v[98:113]
	ds_read_b128 v[4:7], v3 offset:256
	ds_read_b128 v[8:11], v3 offset:288
	s_waitcnt lgkmcnt(1)
	v_mfma_f32_32x32x16_bf16 v[82:97], v[4:7], v[158:161], v[82:97]
	ds_read_b128 v[4:7], v3 offset:13056
	ds_read_b128 v[12:15], v3 offset:13088
	s_waitcnt lgkmcnt(1)
	v_mfma_f32_32x32x16_bf16 v[98:113], v[4:7], v[158:161], v[98:113]
	v_mfma_f32_32x32x16_bf16 v[82:97], v[8:11], v[162:165], v[82:97]
	ds_read_b128 v[4:7], v3 offset:320
	ds_read_b128 v[8:11], v3 offset:352
	s_waitcnt lgkmcnt(2)
	v_mfma_f32_32x32x16_bf16 v[98:113], v[12:15], v[162:165], v[98:113]
	s_waitcnt lgkmcnt(1)
	v_mfma_f32_32x32x16_bf16 v[82:97], v[4:7], v[166:169], v[82:97]
	ds_read_b128 v[4:7], v3 offset:13120
	ds_read_b128 v[12:15], v3 offset:13152
	s_waitcnt lgkmcnt(1)
	v_mfma_f32_32x32x16_bf16 v[98:113], v[4:7], v[166:169], v[98:113]
	v_mfma_f32_32x32x16_bf16 v[82:97], v[8:11], v[130:133], v[82:97]
	s_waitcnt lgkmcnt(0)
	v_mfma_f32_32x32x16_bf16 v[98:113], v[12:15], v[130:133], v[98:113]
	s_add_i32 s0, s84, -1
	s_cmp_le_u32 s0, s2
	s_cbranch_scc1 .LBB0_877
	v_cmp_gt_i32_e64 s[66:67], 26, v216
	v_cmp_gt_i32_e64 s[68:69], 27, v216
	v_cmp_gt_i32_e64 s[64:65], 25, v216
	s_and_b64 s[66:67], s[68:69], s[66:67]
	v_cmp_gt_i32_e64 s[62:63], 24, v216
	s_and_b64 s[64:65], s[66:67], s[64:65]
	v_cmp_gt_i32_e64 s[60:61], 19, v216
	s_and_b64 s[62:63], s[64:65], s[62:63]
	v_cmp_gt_i32_e64 s[58:59], 18, v216
	s_and_b64 s[60:61], s[62:63], s[60:61]
	v_cmp_gt_i32_e64 s[56:57], 17, v216
	s_and_b64 s[58:59], s[60:61], s[58:59]
	v_cmp_gt_i32_e64 s[54:55], 16, v216
	s_and_b64 s[56:57], s[58:59], s[56:57]
	v_cmp_gt_i32_e64 s[52:53], 11, v216
	s_and_b64 s[54:55], s[56:57], s[54:55]
	v_cmp_gt_i32_e64 s[50:51], 10, v216
	s_and_b64 s[52:53], s[54:55], s[52:53]
	v_cmp_gt_i32_e64 s[48:49], 9, v216
	s_and_b64 s[50:51], s[52:53], s[50:51]
	v_cmp_gt_i32_e64 s[46:47], 8, v216
	s_and_b64 s[48:49], s[50:51], s[48:49]
	v_cmp_gt_i32_e64 s[44:45], 3, v216
	s_and_b64 s[46:47], s[48:49], s[46:47]
	v_cmp_gt_i32_e64 s[42:43], 2, v216
	s_and_b64 s[44:45], s[46:47], s[44:45]
	v_cmp_gt_i32_e64 s[38:39], 1, v216
	s_and_b64 s[42:43], s[44:45], s[42:43]
	v_cmp_gt_i32_e64 s[0:1], 0, v216
	s_and_b64 s[38:39], s[42:43], s[38:39]
	s_and_b64 s[0:1], s[38:39], s[0:1]
	v_cmp_gt_i32_e64 s[36:37], 58, v216
	v_cndmask_b32_e64 v82, v82, v213, s[0:1]
	v_cmp_gt_i32_e64 s[0:1], 59, v216
	v_cmp_gt_i32_e64 s[34:35], 57, v216
	v_cmp_gt_i32_e64 s[30:31], 56, v216
	v_cndmask_b32_e64 v113, v113, v213, s[0:1]
	s_and_b64 s[0:1], s[0:1], s[36:37]
	v_cndmask_b32_e64 v112, v112, v213, s[0:1]
	s_and_b64 s[0:1], s[0:1], s[34:35]
	v_cmp_gt_i32_e64 s[28:29], 51, v216
	v_cndmask_b32_e64 v111, v111, v213, s[0:1]
	s_and_b64 s[0:1], s[0:1], s[30:31]
	v_cmp_gt_i32_e64 s[26:27], 50, v216
	v_cndmask_b32_e64 v110, v110, v213, s[0:1]
	s_and_b64 s[0:1], s[0:1], s[28:29]
	v_cmp_gt_i32_e64 s[24:25], 49, v216
	v_cndmask_b32_e64 v109, v109, v213, s[0:1]
	s_and_b64 s[0:1], s[0:1], s[26:27]
	v_cmp_gt_i32_e64 s[22:23], 48, v216
	v_cndmask_b32_e64 v108, v108, v213, s[0:1]
	s_and_b64 s[0:1], s[0:1], s[24:25]
	v_cmp_gt_i32_e64 s[20:21], 43, v216
	v_cndmask_b32_e64 v107, v107, v213, s[0:1]
	s_and_b64 s[0:1], s[0:1], s[22:23]
	v_cmp_gt_i32_e64 s[18:19], 42, v216
	v_cndmask_b32_e64 v106, v106, v213, s[0:1]
	s_and_b64 s[0:1], s[0:1], s[20:21]
	v_cmp_gt_i32_e64 s[16:17], 41, v216
	v_cndmask_b32_e64 v105, v105, v213, s[0:1]
	s_and_b64 s[0:1], s[0:1], s[18:19]
	v_cmp_gt_i32_e64 s[14:15], 40, v216
	v_cndmask_b32_e64 v104, v104, v213, s[0:1]
	s_and_b64 s[0:1], s[0:1], s[16:17]
	v_cmp_gt_i32_e64 s[12:13], 35, v216
	v_cndmask_b32_e64 v103, v103, v213, s[0:1]
	s_and_b64 s[0:1], s[0:1], s[14:15]
	v_cmp_gt_i32_e64 s[10:11], 34, v216
	v_cndmask_b32_e64 v102, v102, v213, s[0:1]
	s_and_b64 s[0:1], s[0:1], s[12:13]
	v_cmp_gt_i32_e64 s[8:9], 33, v216
	v_cndmask_b32_e64 v101, v101, v213, s[0:1]
	s_and_b64 s[0:1], s[0:1], s[10:11]
	v_cmp_gt_i32_e32 vcc, 32, v216
	v_cndmask_b32_e64 v100, v100, v213, s[0:1]
	s_and_b64 s[0:1], s[0:1], s[8:9]
	s_and_b64 vcc, s[0:1], vcc
	v_cndmask_b32_e64 v97, v97, v213, s[68:69]
	v_cndmask_b32_e64 v96, v96, v213, s[66:67]
	v_cndmask_b32_e64 v95, v95, v213, s[64:65]
	v_cndmask_b32_e64 v94, v94, v213, s[62:63]
	v_cndmask_b32_e64 v93, v93, v213, s[60:61]
	v_cndmask_b32_e64 v92, v92, v213, s[58:59]
	v_cndmask_b32_e64 v91, v91, v213, s[56:57]
	v_cndmask_b32_e64 v90, v90, v213, s[54:55]
	v_cndmask_b32_e64 v89, v89, v213, s[52:53]
	v_cndmask_b32_e64 v88, v88, v213, s[50:51]
	v_cndmask_b32_e64 v87, v87, v213, s[48:49]
	v_cndmask_b32_e64 v86, v86, v213, s[46:47]
	v_cndmask_b32_e64 v85, v85, v213, s[44:45]
	v_cndmask_b32_e64 v84, v84, v213, s[42:43]
	v_cndmask_b32_e64 v83, v83, v213, s[38:39]
	v_cndmask_b32_e64 v99, v99, v213, s[0:1]
	v_cndmask_b32_e32 v98, v98, v213, vcc
